# speedup vs baseline: 1.0284x; 1.0057x over previous
_Z8k_layer2PKhPKfPK15HIP_vector_typeIjLj4EEPKjS2_PKDF16_S2_Pf:
	s_lshl_b32 s3, s2, 2
	s_and_b32 s3, s3, 28
	s_and_b32 s12, s2, 0xffffffe0
	s_or_b32 s3, s3, s12
	s_bfe_u32 s12, s2, 0x20003
	s_or_b32 s3, s3, s12
	s_load_dwordx8 s[4:11], s[0:1], 0x0
	s_cmpk_eq_i32 s2, 0x3ef
	s_movk_i32 s12, 0x3f7
	s_cselect_b32 s12, s12, 0x3fb
	s_cmpk_gt_i32 s3, 0x3fc
	s_cselect_b32 s12, s12, s3
	v_lshrrev_b32_e32 v80, 3, v0
	v_lshl_or_b32 v6, s12, 5, v80
	v_ashrrev_i32_e32 v7, 31, v6
	v_or_b32_e32 v83, 0x200, v0
	v_or_b32_e32 v82, 0x300, v0
	s_waitcnt lgkmcnt(0)
	v_lshl_add_u64 v[2:3], v[6:7], 4, s[8:9]
	v_lshlrev_b32_e32 v14, 2, v0
	v_or_b32_e32 v84, 0x100, v0
	v_lshlrev_b32_e32 v7, 2, v83
	v_min_u32_e32 v8, 0x3fc, v82
	global_load_dwordx4 v[2:5], v[2:3], off
	v_lshlrev_b32_e32 v1, 2, v84
	v_lshlrev_b32_e32 v8, 2, v8
	global_load_dword v15, v14, s[6:7]
	global_load_dword v16, v1, s[6:7]
	global_load_dword v17, v7, s[6:7]
	global_load_dword v18, v8, s[6:7]
	s_movk_i32 s13, 0x188
	v_mad_u64_u32 v[6:7], s[8:9], s12, 17, v[6:7]
	v_min_i32_e32 v1, 0xc350, v6
	v_mov_b32_e32 v10, 0xc350
	v_cmp_gt_u32_e32 vcc, s13, v0
	v_lshlrev_b32_e32 v81, 4, v0
	v_and_b32_e32 v60, 0x70, v81
	v_cndmask_b32_e32 v6, v10, v1, vcc
	v_mov_b32_e32 v61, 0
	v_ashrrev_i32_e32 v7, 31, v6
	s_mul_i32 s3, s12, 49
	v_lshl_add_u64 v[8:9], s[4:5], 0, v[60:61]
	v_lshlrev_b64 v[6:7], 7, v[6:7]
	v_lshrrev_b32_e32 v1, 3, v84
	v_lshl_add_u64 v[38:39], v[8:9], 0, v[6:7]
	s_movk_i32 s8, 0x88
	v_add_u32_e32 v6, s3, v1
	v_min_i32_e32 v6, 0xc350, v6
	v_cmp_gt_u32_e32 vcc, s8, v0
	s_ashr_i32 s13, s12, 31
	s_lshl_b64 s[8:9], s[12:13], 2
	v_cndmask_b32_e32 v6, v10, v6, vcc
	v_ashrrev_i32_e32 v7, 31, v6
	v_lshlrev_b64 v[6:7], 7, v[6:7]
	v_lshl_add_u64 v[40:41], v[8:9], 0, v[6:7]
	global_load_dwordx4 v[10:13], v[38:39], off
	global_load_dwordx4 v[6:9], v[40:41], off
	s_add_u32 s8, s6, s8
	s_addc_u32 s9, s7, s9
	s_load_dword s18, s[8:9], 0x0
	s_load_dwordx4 s[12:15], s[0:1], 0x28
	s_load_dwordx2 s[6:7], s[0:1], 0x38
	v_cmp_gt_u32_e32 vcc, 64, v0
	s_waitcnt vmcnt(4)
	v_mul_f32_e32 v15, 0x4b800000, v15
	v_mul_f32_e32 v16, 0x4b800000, v16
	ds_write2st64_b32 v14, v15, v16 offset0:136 offset1:140
	v_and_b32_e32 v105, 7, v0
	v_sub_co_u32_e64 v106, s[22:23], v105, v3
	v_add_u32_e32 v107, v2, v105
	v_add_u32_e32 v106, v106, v4
	v_cndmask_b32_e64 v106, v106, v107, s[22:23]
	v_mov_b32_e32 v107, 0
	v_lshl_add_u64 v[106:107], v[106:107], 2, s[10:11]
	global_load_dword v104, v[106:107], off
	s_waitcnt vmcnt(3)
	v_mul_f32_e32 v17, 0x4b800000, v17
	v_mul_f32_e32 v18, 0x4b800000, v18
	ds_write2st64_b32 v14, v17, v18 offset0:144 offset1:148
	s_and_saveexec_b64 s[8:9], vcc
	s_cbranch_execz .LBB3_4
	v_cmp_gt_u32_e32 vcc, 49, v0
	v_mov_b32_e32 v15, 1.0
	s_and_saveexec_b64 s[16:17], vcc
	s_cbranch_execz .LBB3_3
	s_load_dwordx2 s[0:1], s[0:1], 0x20
	v_add_u32_e32 v15, s3, v0
	v_min_i32_e32 v16, 0xc34f, v15
	v_ashrrev_i32_e32 v17, 31, v16
	s_waitcnt lgkmcnt(0)
	v_lshl_add_u64 v[16:17], v[16:17], 2, s[0:1]
	global_load_dword v16, v[16:17], off
	s_mov_b32 s0, 0xc350
	v_cmp_gt_i32_e32 vcc, s0, v15
	s_waitcnt vmcnt(0)
	s_nop 0
	v_cndmask_b32_e32 v15, 1.0, v16, vcc

.LBB3_4:
	s_or_b64 exec, exec, s[8:9]
	v_and_b32_e32 v47, 7, v0
	v_lshlrev_b32_e32 v49, 2, v47
	v_mul_u32_u24_e32 v14, 0x220, v80
	s_waitcnt vmcnt(2)
	v_cvt_f32_ubyte0_e32 v15, v10
	v_cvt_f32_ubyte1_e32 v16, v10
	v_or_b32_e32 v14, v49, v14
	s_waitcnt lgkmcnt(0)
	v_mul_f32_e32 v15, s18, v15
	v_mul_f32_e32 v16, s18, v16
	ds_write2_b32 v14, v15, v16 offset1:8
	v_cvt_f32_ubyte2_e32 v15, v10
	v_cvt_f32_ubyte3_e32 v10, v10
	v_mul_f32_e32 v15, s18, v15
	v_mul_f32_e32 v10, s18, v10
	ds_write2_b32 v14, v15, v10 offset0:16 offset1:24
	v_cvt_f32_ubyte0_e32 v10, v11
	v_cvt_f32_ubyte1_e32 v15, v11
	v_mul_f32_e32 v10, s18, v10
	v_mul_f32_e32 v15, s18, v15
	ds_write2_b32 v14, v10, v15 offset0:32 offset1:40
	v_cvt_f32_ubyte2_e32 v10, v11
	v_cvt_f32_ubyte3_e32 v11, v11
	v_mul_f32_e32 v10, s18, v10
	v_mul_f32_e32 v11, s18, v11
	ds_write2_b32 v14, v10, v11 offset0:48 offset1:56
	v_cvt_f32_ubyte0_e32 v10, v12
	v_cvt_f32_ubyte1_e32 v11, v12
	v_mul_f32_e32 v10, s18, v10
	v_mul_f32_e32 v11, s18, v11
	ds_write2_b32 v14, v10, v11 offset0:64 offset1:72
	v_cvt_f32_ubyte2_e32 v10, v12
	v_cvt_f32_ubyte3_e32 v11, v12
	v_mul_f32_e32 v10, s18, v10
	v_mul_f32_e32 v11, s18, v11
	ds_write2_b32 v14, v10, v11 offset0:80 offset1:88
	v_cvt_f32_ubyte0_e32 v10, v13
	v_cvt_f32_ubyte1_e32 v11, v13
	v_mul_f32_e32 v10, s18, v10
	v_mul_f32_e32 v11, s18, v11
	ds_write2_b32 v14, v10, v11 offset0:96 offset1:104
	v_cvt_f32_ubyte2_e32 v10, v13
	v_cvt_f32_ubyte3_e32 v11, v13
	v_mul_f32_e32 v10, s18, v10
	v_mul_f32_e32 v11, s18, v11
	ds_write2_b32 v14, v10, v11 offset0:112 offset1:120
	v_mul_u32_u24_e32 v10, 0x220, v1
	s_waitcnt vmcnt(1)
	v_cvt_f32_ubyte0_e32 v11, v6
	v_cvt_f32_ubyte1_e32 v12, v6
	v_or_b32_e32 v10, v49, v10
	v_mul_f32_e32 v11, s18, v11
	v_mul_f32_e32 v12, s18, v12
	ds_write2_b32 v10, v11, v12 offset1:8
	v_cvt_f32_ubyte2_e32 v11, v6
	v_cvt_f32_ubyte3_e32 v6, v6
	v_mul_f32_e32 v11, s18, v11
	v_mul_f32_e32 v6, s18, v6
	ds_write2_b32 v10, v11, v6 offset0:16 offset1:24
	v_cvt_f32_ubyte0_e32 v6, v7
	v_cvt_f32_ubyte1_e32 v11, v7
	v_mul_f32_e32 v6, s18, v6
	v_mul_f32_e32 v11, s18, v11
	ds_write2_b32 v10, v6, v11 offset0:32 offset1:40
	v_cvt_f32_ubyte2_e32 v6, v7
	v_cvt_f32_ubyte3_e32 v7, v7
	v_mul_f32_e32 v6, s18, v6
	v_mul_f32_e32 v7, s18, v7
	ds_write2_b32 v10, v6, v7 offset0:48 offset1:56
	v_cvt_f32_ubyte0_e32 v6, v8
	v_cvt_f32_ubyte1_e32 v7, v8
	v_mul_f32_e32 v6, s18, v6
	v_mul_f32_e32 v7, s18, v7
	ds_write2_b32 v10, v6, v7 offset0:64 offset1:72
	v_cvt_f32_ubyte2_e32 v6, v8
	v_cvt_f32_ubyte3_e32 v7, v8
	v_mul_f32_e32 v6, s18, v6
	v_mul_f32_e32 v7, s18, v7
	ds_write2_b32 v10, v6, v7 offset0:80 offset1:88
	v_cvt_f32_ubyte0_e32 v6, v9
	v_cvt_f32_ubyte1_e32 v7, v9
	v_mul_f32_e32 v6, s18, v6
	v_mul_f32_e32 v7, s18, v7
	ds_write2_b32 v10, v6, v7 offset0:96 offset1:104
	v_cvt_f32_ubyte2_e32 v6, v9
	v_cvt_f32_ubyte3_e32 v7, v9
	v_mul_f32_e32 v6, s18, v6
	v_mul_f32_e32 v7, s18, v7
	ds_write2_b32 v10, v6, v7 offset0:112 offset1:120
	s_waitcnt lgkmcnt(0)
	s_barrier
	s_setprio 2
	s_mov_b32 s24, 0x0c020c00
	s_mov_b32 s25, 0x0c030c01
	v_mov_b32_e32 v65, 0
	v_mbcnt_lo_u32_b32 v7, -1, 0
	v_add_u32_e32 v5, v5, v3
	v_mbcnt_hi_u32_b32 v61, -1, v7
	v_mov_b32_e32 v51, 0x100c350
	v_lshlrev_b32_e32 v15, 2, v61
	v_cmp_lt_u32_e32 vcc, v47, v5
	v_and_b32_e32 v55, 0x1e0, v15
	v_add_u32_e32 v14, 7, v5
	v_mov_b32_e32 v67, v65
	v_mov_b32_e32 v66, v65
	v_mov_b32_e32 v69, v65
	v_mov_b32_e32 v68, v65
	v_mov_b32_e32 v71, v65
	v_mov_b32_e32 v70, v65
	v_mov_b32_e32 v73, v65
	v_mov_b32_e32 v72, v65
	v_mov_b32_e32 v75, v65
	v_mov_b32_e32 v74, v65
	v_mov_b32_e32 v77, v65
	v_mov_b32_e32 v76, v65
	v_mov_b32_e32 v79, v65
	v_mov_b32_e32 v64, v65
	v_mov_b32_e32 v78, v65
	s_waitcnt vmcnt(0)
	v_cndmask_b32_e32 v95, v51, v104, vcc
	ds_bpermute_b32 v9, v55, v95
	ds_bpermute_b32 v8, v55, v95 offset:4
	ds_bpermute_b32 v7, v55, v95 offset:8
	ds_bpermute_b32 v6, v55, v95 offset:12
	v_cmp_lt_u32_e32 vcc, 7, v14
	s_waitcnt lgkmcnt(3)
	v_lshrrev_b32_e32 v98, 16, v9
	s_and_saveexec_b64 s[8:9], vcc
	s_cbranch_execz .LBB3_24
	v_lshlrev_b32_e32 v42, 4, v47
	v_mov_b32_e32 v43, 0
	s_waitcnt lgkmcnt(0)
	v_and_b32_e32 v29, 0xffff, v6
	v_lshl_add_u64 v[44:45], s[4:5], 0, v[42:43]
	v_and_b32_e32 v28, 0xffff, v7
	v_lshlrev_b32_e32 v42, 7, v29
	v_lshl_add_u64 v[16:17], v[44:45], 0, v[42:43]
	v_lshlrev_b32_e32 v42, 7, v28
	v_and_b32_e32 v27, 0xffff, v8
	v_lshl_add_u64 v[18:19], v[44:45], 0, v[42:43]
	v_or_b32_e32 v34, 8, v47
	v_and_b32_e32 v26, 0xffff, v9
	global_load_dwordx4 v[6:9], v[16:17], off
	global_load_dwordx4 v[10:13], v[18:19], off
	v_lshlrev_b32_e32 v42, 7, v27
	v_sub_co_u32_e32 v19, vcc, v34, v3
	v_lshl_add_u64 v[16:17], v[44:45], 0, v[42:43]
	v_lshlrev_b32_e32 v42, 7, v26
	v_add_u32_e32 v18, v2, v34
	v_add_u32_e32 v19, v19, v4
	v_lshl_add_u64 v[22:23], v[44:45], 0, v[42:43]
	v_cndmask_b32_e32 v42, v19, v18, vcc
	v_lshl_add_u64 v[24:25], v[42:43], 2, s[10:11]
	global_load_dword v35, v[24:25], off
	global_load_dwordx4 v[18:21], v[16:17], off
	global_load_dwordx4 v[30:33], v[22:23], off
	s_mov_b32 s19, 0x539782a
	v_lshrrev_b32_e32 v88, 3, v14
	v_mul_hi_u32 v14, v26, s19
	v_or_b32_e32 v93, 28, v15
	v_mul_hi_u32 v15, v27, s19
	v_mul_hi_u32 v16, v28, s19
	v_mul_hi_u32 v17, v29, s19
	v_lshlrev_b32_e32 v14, 2, v14
	v_lshlrev_b32_e32 v15, 2, v15
	v_lshlrev_b32_e32 v16, 2, v16
	v_lshlrev_b32_e32 v17, 2, v17
	ds_read_b32 v56, v14 offset:34816
	ds_read_b32 v57, v15 offset:34816
	ds_read_b32 v50, v16 offset:34816
	ds_read_b32 v46, v17 offset:34816
	v_cmp_lt_u32_e64 s[0:1], v34, v5
	v_or_b32_e32 v85, 4, v55
	v_or_b32_e32 v86, 8, v55
	v_or_b32_e32 v87, 12, v55
	v_sub_u32_e32 v89, v4, v3
	v_cmp_eq_u32_e32 vcc, 0, v47
	v_and_b32_e32 v4, 56, v61
	v_or_b32_e32 v90, 16, v55
	v_or_b32_e32 v91, 20, v55
	v_or_b32_e32 v92, 24, v55
	v_or_b32_e32 v94, 16, v47
	s_mov_b64 s[16:17], 0
	s_mov_b32 s20, 0x1000000
	v_mov_b32_e32 v78, v43
	v_mov_b32_e32 v79, v43
	v_mov_b32_e32 v76, v43
	v_mov_b32_e32 v77, v43
	v_mov_b32_e32 v74, v43
	v_mov_b32_e32 v75, v43
	v_mov_b32_e32 v72, v43
	v_mov_b32_e32 v73, v43
	v_mov_b32_e32 v70, v43
	v_mov_b32_e32 v71, v43
	v_mov_b32_e32 v68, v43
	v_mov_b32_e32 v69, v43
	v_mov_b32_e32 v66, v43
	v_mov_b32_e32 v67, v43
	v_mov_b32_e32 v64, v43
	v_mov_b32_e32 v65, v43
	s_waitcnt vmcnt(2)
	v_cndmask_b32_e64 v96, v51, v35, s[0:1]
	s_branch .LBB3_7
.LBB3_6:
	s_or_b64 exec, exec, s[4:5]
	s_waitcnt vmcnt(4)
	v_perm_b32 v112, v14, v14, s24
	v_perm_b32 v113, v14, v14, s25
	v_perm_b32 v114, v15, v15, s24
	v_perm_b32 v115, v15, v15, s25
	v_perm_b32 v116, v16, v16, s24
	v_perm_b32 v117, v16, v16, s25
	v_cmp_lt_u32_e64 s[0:1], v94, v5
	v_add_u32_e32 v88, -1, v88
	v_perm_b32 v118, v17, v17, s24
	v_perm_b32 v119, v17, v17, s25
	v_fma_mix_f32 v68, v116, v48, v68 op_sel:[1,0,0] op_sel_hi:[1,0,0]
	v_fma_mix_f32 v69, v117, v48, v69 op_sel:[1,0,0] op_sel_hi:[1,0,0]
	v_fma_mix_f32 v70, v116, v48, v62 op_sel_hi:[1,0,0]
	v_fma_mix_f32 v71, v117, v48, v63 op_sel_hi:[1,0,0]
	v_cndmask_b32_e64 v14, v51, v97, s[0:1]
	v_cmp_eq_u32_e64 s[0:1], 0, v88
	v_fma_mix_f32 v64, v118, v48, v24 op_sel:[1,0,0] op_sel_hi:[1,0,0]
	v_fma_mix_f32 v65, v119, v48, v25 op_sel:[1,0,0] op_sel_hi:[1,0,0]
	v_fma_mix_f32 v66, v118, v48, v36 op_sel_hi:[1,0,0]
	v_fma_mix_f32 v67, v119, v48, v37 op_sel_hi:[1,0,0]
	v_fma_mix_f32 v72, v114, v48, v22 op_sel:[1,0,0] op_sel_hi:[1,0,0]
	v_fma_mix_f32 v73, v115, v48, v23 op_sel:[1,0,0] op_sel_hi:[1,0,0]
	v_fma_mix_f32 v74, v114, v48, v58 op_sel_hi:[1,0,0]
	v_fma_mix_f32 v75, v115, v48, v59 op_sel_hi:[1,0,0]
	v_fma_mix_f32 v76, v112, v48, v34 op_sel:[1,0,0] op_sel_hi:[1,0,0]
	v_fma_mix_f32 v77, v113, v48, v35 op_sel:[1,0,0] op_sel_hi:[1,0,0]
	v_fma_mix_f32 v78, v112, v48, v28 op_sel_hi:[1,0,0]
	v_fma_mix_f32 v79, v113, v48, v29 op_sel_hi:[1,0,0]
	v_add_u32_e32 v94, 8, v94
	s_or_b64 s[16:17], s[0:1], s[16:17]
	v_mov_b32_e32 v95, v96
	v_mov_b32_e32 v96, v14
	s_andn2_b64 exec, exec, s[16:17]
	s_cbranch_execz .LBB3_23

.LBB3_9:
	s_or_b64 exec, exec, s[4:5]
	s_waitcnt vmcnt(5)
	v_perm_b32 v120, v30, v30, s24
	v_perm_b32 v121, v30, v30, s25
	v_fma_mix_f32 v78, v120, v56, v78 op_sel_hi:[1,0,0]
	v_fma_mix_f32 v79, v121, v56, v79 op_sel_hi:[1,0,0]
	v_fma_mix_f32 v76, v120, v56, v76 op_sel:[1,0,0] op_sel_hi:[1,0,0]
	v_fma_mix_f32 v77, v121, v56, v77 op_sel:[1,0,0] op_sel_hi:[1,0,0]
	v_perm_b32 v122, v31, v31, s24
	v_perm_b32 v123, v31, v31, s25
	v_fma_mix_f32 v74, v122, v56, v74 op_sel_hi:[1,0,0]
	v_fma_mix_f32 v75, v123, v56, v75 op_sel_hi:[1,0,0]
	v_perm_b32 v124, v32, v32, s24
	v_perm_b32 v125, v32, v32, s25
	v_fma_mix_f32 v70, v124, v56, v70 op_sel_hi:[1,0,0]
	v_fma_mix_f32 v71, v125, v56, v71 op_sel_hi:[1,0,0]
	v_fma_mix_f32 v68, v124, v56, v68 op_sel:[1,0,0] op_sel_hi:[1,0,0]
	v_fma_mix_f32 v69, v125, v56, v69 op_sel:[1,0,0] op_sel_hi:[1,0,0]
	v_perm_b32 v126, v33, v33, s24
	v_perm_b32 v127, v33, v33, s25
	v_fma_mix_f32 v66, v126, v56, v66 op_sel_hi:[1,0,0]
	v_fma_mix_f32 v67, v127, v56, v67 op_sel_hi:[1,0,0]
	v_and_b32_e32 v32, 2, v52
	v_fma_mix_f32 v72, v122, v56, v72 op_sel:[1,0,0] op_sel_hi:[1,0,0]
	v_fma_mix_f32 v73, v123, v56, v73 op_sel:[1,0,0] op_sel_hi:[1,0,0]
	v_fma_mix_f32 v30, v126, v56, v64 op_sel:[1,0,0] op_sel_hi:[1,0,0]
	v_fma_mix_f32 v31, v127, v56, v65 op_sel:[1,0,0] op_sel_hi:[1,0,0]
	v_cmp_ne_u32_e64 s[0:1], 0, v32
	s_and_saveexec_b64 s[4:5], s[0:1]
	s_cbranch_execz .LBB3_11
	v_and_b32_e32 v32, 63, v98
	v_mul_u32_u24_e32 v32, 0x220, v32
	v_or_b32_e32 v42, v49, v32
	ds_read2_b32 v[32:33], v42 offset1:8
	ds_read2_b32 v[64:65], v42 offset0:16 offset1:24
	ds_read2_b32 v[98:99], v42 offset0:32 offset1:40
	ds_bpermute_b32 v63, v85, v95
	s_waitcnt lgkmcnt(3)
	v_add_f32_e32 v32, v78, v32
	v_add_f32_e32 v33, v79, v33
	s_waitcnt lgkmcnt(2)
	v_add_f32_e32 v53, v76, v64
	ds_write2_b32 v42, v32, v33 offset1:8
	v_add_f32_e32 v32, v77, v65
	ds_write2_b32 v42, v53, v32 offset0:16 offset1:24
	ds_read2_b32 v[32:33], v42 offset0:48 offset1:56
	ds_read2_b32 v[64:65], v42 offset0:64 offset1:72
	s_waitcnt lgkmcnt(5)
	v_add_f32_e32 v53, v74, v98
	v_add_f32_e32 v59, v75, v99
	ds_write2_b32 v42, v53, v59 offset0:32 offset1:40
	s_waitcnt lgkmcnt(2)
	v_add_f32_e32 v32, v72, v32
	v_add_f32_e32 v33, v73, v33
	ds_write2_b32 v42, v32, v33 offset0:48 offset1:56
	ds_read2_b32 v[32:33], v42 offset0:80 offset1:88
	s_waitcnt lgkmcnt(3)
	v_add_f32_e32 v53, v70, v64
	v_add_f32_e32 v59, v71, v65
	ds_read2_b32 v[64:65], v42 offset0:96 offset1:104
	ds_write2_b32 v42, v53, v59 offset0:64 offset1:72
	s_waitcnt lgkmcnt(2)
	v_add_f32_e32 v32, v68, v32
	v_add_f32_e32 v33, v69, v33
	ds_write2_b32 v42, v32, v33 offset0:80 offset1:88
	ds_read2_b32 v[32:33], v42 offset0:112 offset1:120
	s_waitcnt lgkmcnt(3)
	v_add_f32_e32 v53, v66, v64
	v_add_f32_e32 v59, v67, v65
	v_lshrrev_b32_e32 v98, 16, v63
	ds_write2_b32 v42, v53, v59 offset0:96 offset1:104
	s_waitcnt lgkmcnt(1)
	v_add_f32_e32 v30, v30, v32
	v_add_f32_e32 v31, v31, v33
	ds_write2_b32 v42, v30, v31 offset0:112 offset1:120
	v_mov_b32_e32 v30, 0
	v_mov_b32_e32 v31, v30
	v_mov_b32_e32 v66, v30
	v_mov_b32_e32 v67, v30
	v_mov_b32_e32 v68, v30
	v_mov_b32_e32 v69, v30
	v_mov_b32_e32 v70, v30
	v_mov_b32_e32 v71, v30
	v_mov_b32_e32 v72, v30
	v_mov_b32_e32 v73, v30
	v_mov_b32_e32 v74, v30
	v_mov_b32_e32 v75, v30
	v_mov_b32_e32 v76, v30
	v_mov_b32_e32 v77, v30
	v_mov_b32_e32 v78, v30
	v_mov_b32_e32 v79, v30
.LBB3_11:
	s_or_b64 exec, exec, s[4:5]
	v_perm_b32 v112, v18, v18, s24
	v_perm_b32 v113, v18, v18, s25
	v_fma_mix_f32 v78, v112, v57, v78 op_sel_hi:[1,0,0]
	v_fma_mix_f32 v79, v113, v57, v79 op_sel_hi:[1,0,0]
	v_fma_mix_f32 v76, v112, v57, v76 op_sel:[1,0,0] op_sel_hi:[1,0,0]
	v_fma_mix_f32 v77, v113, v57, v77 op_sel:[1,0,0] op_sel_hi:[1,0,0]
	v_perm_b32 v114, v19, v19, s24
	v_perm_b32 v115, v19, v19, s25
	v_fma_mix_f32 v74, v114, v57, v74 op_sel_hi:[1,0,0]
	v_fma_mix_f32 v75, v115, v57, v75 op_sel_hi:[1,0,0]
	v_perm_b32 v116, v20, v20, s24
	v_perm_b32 v117, v20, v20, s25
	v_fma_mix_f32 v70, v116, v57, v70 op_sel_hi:[1,0,0]
	v_fma_mix_f32 v71, v117, v57, v71 op_sel_hi:[1,0,0]
	v_fma_mix_f32 v64, v116, v57, v68 op_sel:[1,0,0] op_sel_hi:[1,0,0]
	v_fma_mix_f32 v65, v117, v57, v69 op_sel:[1,0,0] op_sel_hi:[1,0,0]
	v_perm_b32 v118, v21, v21, s24
	v_perm_b32 v119, v21, v21, s25
	v_fma_mix_f32 v72, v114, v57, v72 op_sel:[1,0,0] op_sel_hi:[1,0,0]
	v_fma_mix_f32 v73, v115, v57, v73 op_sel:[1,0,0] op_sel_hi:[1,0,0]
	v_fma_mix_f32 v32, v118, v57, v66 op_sel_hi:[1,0,0]
	v_fma_mix_f32 v33, v119, v57, v67 op_sel_hi:[1,0,0]
	v_and_b32_e32 v20, 4, v52
	v_fma_mix_f32 v18, v118, v57, v30 op_sel:[1,0,0] op_sel_hi:[1,0,0]
	v_fma_mix_f32 v19, v119, v57, v31 op_sel:[1,0,0] op_sel_hi:[1,0,0]
	v_cmp_ne_u32_e64 s[0:1], 0, v20
	s_and_saveexec_b64 s[4:5], s[0:1]
	s_cbranch_execz .LBB3_13
	v_and_b32_e32 v20, 63, v98
	v_mul_u32_u24_e32 v20, 0x220, v20
	v_or_b32_e32 v42, v49, v20
	ds_read2_b32 v[20:21], v42 offset1:8
	ds_read2_b32 v[30:31], v42 offset0:16 offset1:24
	ds_read2_b32 v[56:57], v42 offset0:32 offset1:40
	s_waitcnt lgkmcnt(2)
	v_add_f32_e32 v20, v78, v20
	v_add_f32_e32 v21, v79, v21
	s_waitcnt lgkmcnt(1)
	v_add_f32_e32 v30, v76, v30
	ds_write2_b32 v42, v20, v21 offset1:8
	v_add_f32_e32 v20, v77, v31
	ds_write2_b32 v42, v30, v20 offset0:16 offset1:24
	ds_read2_b32 v[20:21], v42 offset0:48 offset1:56
	s_waitcnt lgkmcnt(3)
	v_add_f32_e32 v30, v74, v56
	v_add_f32_e32 v31, v75, v57
	ds_write2_b32 v42, v30, v31 offset0:32 offset1:40
	ds_read2_b32 v[30:31], v42 offset0:64 offset1:72
	s_waitcnt lgkmcnt(2)
	v_add_f32_e32 v20, v72, v20
	v_add_f32_e32 v21, v73, v21
	ds_write2_b32 v42, v20, v21 offset0:48 offset1:56
	ds_read2_b32 v[20:21], v42 offset0:80 offset1:88
	s_waitcnt lgkmcnt(2)
	v_add_f32_e32 v30, v70, v30
	v_add_f32_e32 v31, v71, v31
	ds_write2_b32 v42, v30, v31 offset0:64 offset1:72
	ds_read2_b32 v[30:31], v42 offset0:96 offset1:104
	s_waitcnt lgkmcnt(2)
	v_add_f32_e32 v20, v64, v20
	v_add_f32_e32 v21, v65, v21
	ds_write2_b32 v42, v20, v21 offset0:80 offset1:88
	ds_read2_b32 v[20:21], v42 offset0:112 offset1:120
	s_waitcnt lgkmcnt(2)
	v_add_f32_e32 v30, v32, v30
	ds_bpermute_b32 v32, v86, v95
	v_add_f32_e32 v31, v33, v31
	ds_write2_b32 v42, v30, v31 offset0:96 offset1:104
	s_waitcnt lgkmcnt(2)
	v_add_f32_e32 v18, v18, v20
	v_add_f32_e32 v19, v19, v21
	ds_write2_b32 v42, v18, v19 offset0:112 offset1:120
	v_mov_b32_e32 v18, 0
	s_waitcnt lgkmcnt(2)
	v_lshrrev_b32_e32 v98, 16, v32
	v_mov_b32_e32 v19, v18
	v_mov_b32_e32 v32, v18
	v_mov_b32_e32 v33, v18
	v_mov_b32_e32 v64, v18
	v_mov_b32_e32 v65, v18
	v_mov_b32_e32 v70, v18
	v_mov_b32_e32 v71, v18
	v_mov_b32_e32 v72, v18
	v_mov_b32_e32 v73, v18
	v_mov_b32_e32 v74, v18
	v_mov_b32_e32 v75, v18
	v_mov_b32_e32 v76, v18
	v_mov_b32_e32 v77, v18
	v_mov_b32_e32 v78, v18
	v_mov_b32_e32 v79, v18
.LBB3_13:
	s_or_b64 exec, exec, s[4:5]
	v_perm_b32 v120, v10, v10, s24
	v_perm_b32 v121, v10, v10, s25
	v_fma_mix_f32 v78, v120, v50, v78 op_sel_hi:[1,0,0]
	v_fma_mix_f32 v79, v121, v50, v79 op_sel_hi:[1,0,0]
	v_fma_mix_f32 v76, v120, v50, v76 op_sel:[1,0,0] op_sel_hi:[1,0,0]
	v_fma_mix_f32 v77, v121, v50, v77 op_sel:[1,0,0] op_sel_hi:[1,0,0]
	v_perm_b32 v122, v11, v11, s24
	v_perm_b32 v123, v11, v11, s25
	v_fma_mix_f32 v68, v122, v50, v74 op_sel_hi:[1,0,0]
	v_fma_mix_f32 v69, v123, v50, v75 op_sel_hi:[1,0,0]
	v_perm_b32 v124, v12, v12, s24
	v_perm_b32 v125, v12, v12, s25
	v_fma_mix_f32 v56, v124, v50, v70 op_sel_hi:[1,0,0]
	v_fma_mix_f32 v57, v125, v50, v71 op_sel_hi:[1,0,0]
	v_fma_mix_f32 v30, v124, v50, v64 op_sel:[1,0,0] op_sel_hi:[1,0,0]
	v_fma_mix_f32 v31, v125, v50, v65 op_sel:[1,0,0] op_sel_hi:[1,0,0]
	v_perm_b32 v126, v13, v13, s24
	v_perm_b32 v127, v13, v13, s25
	v_fma_mix_f32 v66, v122, v50, v72 op_sel:[1,0,0] op_sel_hi:[1,0,0]
	v_fma_mix_f32 v67, v123, v50, v73 op_sel:[1,0,0] op_sel_hi:[1,0,0]
	v_fma_mix_f32 v20, v126, v50, v32 op_sel_hi:[1,0,0]
	v_fma_mix_f32 v21, v127, v50, v33 op_sel_hi:[1,0,0]
	v_and_b32_e32 v12, 8, v52
	v_fma_mix_f32 v10, v126, v50, v18 op_sel:[1,0,0] op_sel_hi:[1,0,0]
	v_fma_mix_f32 v11, v127, v50, v19 op_sel:[1,0,0] op_sel_hi:[1,0,0]
	v_cmp_ne_u32_e64 s[0:1], 0, v12
	s_and_saveexec_b64 s[4:5], s[0:1]
	s_cbranch_execz .LBB3_15
	v_and_b32_e32 v12, 63, v98
	v_mul_u32_u24_e32 v12, 0x220, v12
	v_or_b32_e32 v42, v49, v12
	ds_read2_b32 v[12:13], v42 offset1:8
	ds_read2_b32 v[18:19], v42 offset0:16 offset1:24
	ds_read2_b32 v[32:33], v42 offset0:32 offset1:40
	s_waitcnt lgkmcnt(2)
	v_add_f32_e32 v12, v78, v12
	v_add_f32_e32 v13, v79, v13
	s_waitcnt lgkmcnt(1)
	v_add_f32_e32 v18, v76, v18
	ds_write2_b32 v42, v12, v13 offset1:8
	v_add_f32_e32 v12, v77, v19
	ds_write2_b32 v42, v18, v12 offset0:16 offset1:24
	ds_read2_b32 v[12:13], v42 offset0:48 offset1:56
	s_waitcnt lgkmcnt(3)
	v_add_f32_e32 v18, v68, v32
	v_add_f32_e32 v19, v69, v33
	ds_write2_b32 v42, v18, v19 offset0:32 offset1:40
	ds_read2_b32 v[18:19], v42 offset0:64 offset1:72
	s_waitcnt lgkmcnt(2)
	v_add_f32_e32 v12, v66, v12
	v_add_f32_e32 v13, v67, v13
	ds_write2_b32 v42, v12, v13 offset0:48 offset1:56
	ds_read2_b32 v[12:13], v42 offset0:80 offset1:88
	s_waitcnt lgkmcnt(2)
	v_add_f32_e32 v18, v56, v18
	v_add_f32_e32 v19, v57, v19
	ds_write2_b32 v42, v18, v19 offset0:64 offset1:72
	ds_read2_b32 v[18:19], v42 offset0:96 offset1:104
	s_waitcnt lgkmcnt(2)
	v_add_f32_e32 v12, v30, v12
	v_add_f32_e32 v13, v31, v13
	ds_write2_b32 v42, v12, v13 offset0:80 offset1:88
	ds_read2_b32 v[12:13], v42 offset0:112 offset1:120
	s_waitcnt lgkmcnt(2)
	v_add_f32_e32 v18, v20, v18
	ds_bpermute_b32 v20, v87, v95
	v_add_f32_e32 v19, v21, v19
	ds_write2_b32 v42, v18, v19 offset0:96 offset1:104
	s_waitcnt lgkmcnt(2)
	v_add_f32_e32 v10, v10, v12
	v_add_f32_e32 v11, v11, v13
	ds_write2_b32 v42, v10, v11 offset0:112 offset1:120
	v_mov_b32_e32 v10, 0
	s_waitcnt lgkmcnt(2)
	v_lshrrev_b32_e32 v98, 16, v20
	v_mov_b32_e32 v11, v10
	v_mov_b32_e32 v20, v10
	v_mov_b32_e32 v21, v10
	v_mov_b32_e32 v30, v10
	v_mov_b32_e32 v31, v10
	v_mov_b32_e32 v56, v10
	v_mov_b32_e32 v57, v10
	v_mov_b32_e32 v66, v10
	v_mov_b32_e32 v67, v10
	v_mov_b32_e32 v68, v10
	v_mov_b32_e32 v69, v10
	v_mov_b32_e32 v76, v10
	v_mov_b32_e32 v77, v10
	v_mov_b32_e32 v78, v10
	v_mov_b32_e32 v79, v10
.LBB3_15:
	s_or_b64 exec, exec, s[4:5]
	v_perm_b32 v112, v6, v6, s24
	v_perm_b32 v113, v6, v6, s25
	v_fma_mix_f32 v78, v112, v46, v78 op_sel_hi:[1,0,0]
	v_fma_mix_f32 v79, v113, v46, v79 op_sel_hi:[1,0,0]
	v_fma_mix_f32 v76, v112, v46, v76 op_sel:[1,0,0] op_sel_hi:[1,0,0]
	v_fma_mix_f32 v77, v113, v46, v77 op_sel:[1,0,0] op_sel_hi:[1,0,0]
	v_perm_b32 v114, v7, v7, s24
	v_perm_b32 v115, v7, v7, s25
	v_fma_mix_f32 v74, v114, v46, v68 op_sel_hi:[1,0,0]
	v_fma_mix_f32 v75, v115, v46, v69 op_sel_hi:[1,0,0]
	v_perm_b32 v116, v8, v8, s24
	v_perm_b32 v117, v8, v8, s25
	v_fma_mix_f32 v70, v116, v46, v56 op_sel_hi:[1,0,0]
	v_fma_mix_f32 v71, v117, v46, v57 op_sel_hi:[1,0,0]
	v_fma_mix_f32 v68, v116, v46, v30 op_sel:[1,0,0] op_sel_hi:[1,0,0]
	v_fma_mix_f32 v69, v117, v46, v31 op_sel:[1,0,0] op_sel_hi:[1,0,0]
	v_perm_b32 v118, v9, v9, s24
	v_perm_b32 v119, v9, v9, s25
	v_fma_mix_f32 v72, v114, v46, v66 op_sel:[1,0,0] op_sel_hi:[1,0,0]
	v_fma_mix_f32 v73, v115, v46, v67 op_sel:[1,0,0] op_sel_hi:[1,0,0]
	v_fma_mix_f32 v66, v118, v46, v20 op_sel_hi:[1,0,0]
	v_fma_mix_f32 v67, v119, v46, v21 op_sel_hi:[1,0,0]
	v_fma_mix_f32 v64, v118, v46, v10 op_sel:[1,0,0] op_sel_hi:[1,0,0]
	v_fma_mix_f32 v65, v119, v46, v11 op_sel:[1,0,0] op_sel_hi:[1,0,0]
	s_setprio 3
	ds_bpermute_b32 v6, v55, v96
	ds_bpermute_b32 v7, v85, v96
	ds_bpermute_b32 v8, v86, v96
	ds_bpermute_b32 v9, v87, v96
	s_waitcnt lgkmcnt(3)
	v_and_b32_e32 v46, 0xffff, v6
	s_waitcnt lgkmcnt(2)
	v_and_b32_e32 v50, 0xffff, v7
	v_lshlrev_b32_e32 v42, 7, v46
	v_lshl_add_u64 v[6:7], v[44:45], 0, v[42:43]
	v_lshlrev_b32_e32 v42, 7, v50
	s_waitcnt lgkmcnt(1)
	v_and_b32_e32 v53, 0xffff, v8
	global_load_dwordx4 v[30:33], v[6:7], off
	v_lshl_add_u64 v[6:7], v[44:45], 0, v[42:43]
	v_lshlrev_b32_e32 v42, 7, v53
	s_waitcnt lgkmcnt(0)
	v_and_b32_e32 v59, 0xffff, v9
	global_load_dwordx4 v[18:21], v[6:7], off
	v_lshl_add_u64 v[6:7], v[44:45], 0, v[42:43]
	v_lshlrev_b32_e32 v42, 7, v59
	global_load_dwordx4 v[10:13], v[6:7], off
	v_lshl_add_u64 v[6:7], v[44:45], 0, v[42:43]
	global_load_dwordx4 v[6:9], v[6:7], off
	v_mul_hi_u32 v42, v46, s19
	v_lshlrev_b32_e32 v42, 2, v42
	ds_read_b32 v56, v42 offset:34816
	v_mul_hi_u32 v42, v50, s19
	v_lshlrev_b32_e32 v42, 2, v42
	ds_read_b32 v57, v42 offset:34816
	v_mul_hi_u32 v42, v53, s19
	v_lshlrev_b32_e32 v42, 2, v42
	ds_read_b32 v50, v42 offset:34816
	v_mul_hi_u32 v42, v59, s19
	v_lshlrev_b32_e32 v42, 2, v42
	ds_read_b32 v46, v42 offset:34816
	s_setprio 1
	v_and_b32_e32 v42, 16, v52
	v_cmp_ne_u32_e64 s[0:1], 0, v42
	s_and_saveexec_b64 s[4:5], s[0:1]
	s_cbranch_execz .LBB3_17
	v_and_b32_e32 v42, 63, v98
	v_mul_u32_u24_e32 v42, 0x220, v42
	v_or_b32_e32 v42, v49, v42
	ds_read2_b32 v[98:99], v42 offset1:8
	ds_read2_b32 v[100:101], v42 offset0:16 offset1:24
	ds_read2_b32 v[102:103], v42 offset0:32 offset1:40
	s_waitcnt lgkmcnt(2)
	v_add_f32_e32 v53, v78, v98
	v_add_f32_e32 v59, v79, v99
	s_waitcnt lgkmcnt(1)
	v_add_f32_e32 v63, v76, v100
	ds_write2_b32 v42, v53, v59 offset1:8
	v_add_f32_e32 v53, v77, v101
	ds_read2_b32 v[76:77], v42 offset0:48 offset1:56
	ds_write2_b32 v42, v63, v53 offset0:16 offset1:24
	s_waitcnt lgkmcnt(3)
	v_add_f32_e32 v53, v74, v102
	v_add_f32_e32 v59, v75, v103
	ds_read2_b32 v[74:75], v42 offset0:64 offset1:72
	ds_write2_b32 v42, v53, v59 offset0:32 offset1:40
	s_waitcnt lgkmcnt(3)
	v_add_f32_e32 v53, v72, v76
	v_add_f32_e32 v59, v73, v77
	ds_read2_b32 v[72:73], v42 offset0:80 offset1:88
	ds_write2_b32 v42, v53, v59 offset0:48 offset1:56
	s_waitcnt lgkmcnt(3)
	v_add_f32_e32 v53, v70, v74
	v_add_f32_e32 v59, v71, v75
	ds_read2_b32 v[70:71], v42 offset0:96 offset1:104
	ds_write2_b32 v42, v53, v59 offset0:64 offset1:72
	s_waitcnt lgkmcnt(3)
	v_add_f32_e32 v53, v68, v72
	v_add_f32_e32 v59, v69, v73
	ds_read2_b32 v[68:69], v42 offset0:112 offset1:120
	ds_bpermute_b32 v63, v90, v95
	ds_write2_b32 v42, v53, v59 offset0:80 offset1:88
	s_waitcnt lgkmcnt(4)
	v_add_f32_e32 v53, v66, v70
	v_add_f32_e32 v59, v67, v71
	ds_write2_b32 v42, v53, v59 offset0:96 offset1:104
	s_waitcnt lgkmcnt(3)
	v_add_f32_e32 v53, v64, v68
	v_mov_b32_e32 v64, 0
	v_add_f32_e32 v59, v65, v69
	s_waitcnt lgkmcnt(2)
	v_lshrrev_b32_e32 v98, 16, v63
	v_mov_b32_e32 v65, v64
	v_mov_b32_e32 v78, v64
	v_mov_b32_e32 v79, v64
	v_mov_b32_e32 v76, v64
	v_mov_b32_e32 v77, v64
	v_mov_b32_e32 v74, v64
	v_mov_b32_e32 v75, v64
	v_mov_b32_e32 v72, v64
	v_mov_b32_e32 v73, v64
	v_mov_b32_e32 v70, v64
	v_mov_b32_e32 v71, v64
	v_mov_b32_e32 v68, v64
	v_mov_b32_e32 v69, v64
	v_mov_b32_e32 v66, v64
	v_mov_b32_e32 v67, v64
	ds_write2_b32 v42, v53, v59 offset0:112 offset1:120
.LBB3_17:
	s_or_b64 exec, exec, s[4:5]
	s_waitcnt vmcnt(7)
	v_perm_b32 v120, v34, v34, s24
	v_perm_b32 v121, v34, v34, s25
	v_fma_mix_f32 v78, v120, v62, v78 op_sel_hi:[1,0,0]
	v_fma_mix_f32 v79, v121, v62, v79 op_sel_hi:[1,0,0]
	v_fma_mix_f32 v76, v120, v62, v76 op_sel:[1,0,0] op_sel_hi:[1,0,0]
	v_fma_mix_f32 v77, v121, v62, v77 op_sel:[1,0,0] op_sel_hi:[1,0,0]
	v_perm_b32 v122, v35, v35, s24
	v_perm_b32 v123, v35, v35, s25
	v_fma_mix_f32 v74, v122, v62, v74 op_sel_hi:[1,0,0]
	v_fma_mix_f32 v75, v123, v62, v75 op_sel_hi:[1,0,0]
	v_perm_b32 v124, v36, v36, s24
	v_perm_b32 v125, v36, v36, s25
	v_fma_mix_f32 v70, v124, v62, v70 op_sel_hi:[1,0,0]
	v_fma_mix_f32 v71, v125, v62, v71 op_sel_hi:[1,0,0]
	v_fma_mix_f32 v68, v124, v62, v68 op_sel:[1,0,0] op_sel_hi:[1,0,0]
	v_fma_mix_f32 v69, v125, v62, v69 op_sel:[1,0,0] op_sel_hi:[1,0,0]
	v_perm_b32 v126, v37, v37, s24
	v_perm_b32 v127, v37, v37, s25
	v_fma_mix_f32 v66, v126, v62, v66 op_sel_hi:[1,0,0]
	v_fma_mix_f32 v67, v127, v62, v67 op_sel_hi:[1,0,0]
	v_and_b32_e32 v36, 32, v52
	v_fma_mix_f32 v72, v122, v62, v72 op_sel:[1,0,0] op_sel_hi:[1,0,0]
	v_fma_mix_f32 v73, v123, v62, v73 op_sel:[1,0,0] op_sel_hi:[1,0,0]
	v_fma_mix_f32 v34, v126, v62, v64 op_sel:[1,0,0] op_sel_hi:[1,0,0]
	v_fma_mix_f32 v35, v127, v62, v65 op_sel:[1,0,0] op_sel_hi:[1,0,0]
	v_cmp_ne_u32_e64 s[0:1], 0, v36
	s_and_saveexec_b64 s[4:5], s[0:1]
	s_cbranch_execz .LBB3_19
	v_and_b32_e32 v36, 63, v98
	v_mul_u32_u24_e32 v36, 0x220, v36
	v_or_b32_e32 v42, v49, v36
	ds_read2_b32 v[36:37], v42 offset1:8
	ds_read2_b32 v[62:63], v42 offset0:16 offset1:24
	ds_read2_b32 v[64:65], v42 offset0:32 offset1:40
	s_waitcnt lgkmcnt(2)
	v_add_f32_e32 v36, v78, v36
	v_add_f32_e32 v37, v79, v37
	s_waitcnt lgkmcnt(1)
	v_add_f32_e32 v53, v76, v62
	ds_write2_b32 v42, v36, v37 offset1:8
	v_add_f32_e32 v36, v77, v63
	ds_write2_b32 v42, v53, v36 offset0:16 offset1:24
	ds_read2_b32 v[36:37], v42 offset0:48 offset1:56
	ds_read2_b32 v[62:63], v42 offset0:64 offset1:72
	s_waitcnt lgkmcnt(4)
	v_add_f32_e32 v53, v74, v64
	v_add_f32_e32 v59, v75, v65
	ds_write2_b32 v42, v53, v59 offset0:32 offset1:40
	s_waitcnt lgkmcnt(2)
	v_add_f32_e32 v36, v72, v36
	v_add_f32_e32 v37, v73, v37
	ds_write2_b32 v42, v36, v37 offset0:48 offset1:56
	ds_read2_b32 v[36:37], v42 offset0:80 offset1:88
	s_waitcnt lgkmcnt(3)
	v_add_f32_e32 v53, v70, v62
	v_add_f32_e32 v59, v71, v63
	ds_read2_b32 v[62:63], v42 offset0:96 offset1:104
	ds_write2_b32 v42, v53, v59 offset0:64 offset1:72
	s_waitcnt lgkmcnt(2)
	v_add_f32_e32 v36, v68, v36
	v_add_f32_e32 v37, v69, v37
	ds_write2_b32 v42, v36, v37 offset0:80 offset1:88
	ds_read2_b32 v[36:37], v42 offset0:112 offset1:120
	s_waitcnt lgkmcnt(3)
	v_add_f32_e32 v53, v66, v62
	ds_bpermute_b32 v62, v91, v95
	v_add_f32_e32 v59, v67, v63
	ds_write2_b32 v42, v53, v59 offset0:96 offset1:104
	s_waitcnt lgkmcnt(2)
	v_add_f32_e32 v34, v34, v36
	v_add_f32_e32 v35, v35, v37
	ds_write2_b32 v42, v34, v35 offset0:112 offset1:120
	v_mov_b32_e32 v34, 0
	s_waitcnt lgkmcnt(2)
	v_lshrrev_b32_e32 v98, 16, v62
	v_mov_b32_e32 v35, v34
	v_mov_b32_e32 v66, v34
	v_mov_b32_e32 v67, v34
	v_mov_b32_e32 v68, v34
	v_mov_b32_e32 v69, v34
	v_mov_b32_e32 v70, v34
	v_mov_b32_e32 v71, v34
	v_mov_b32_e32 v72, v34
	v_mov_b32_e32 v73, v34
	v_mov_b32_e32 v74, v34
	v_mov_b32_e32 v75, v34
	v_mov_b32_e32 v76, v34
	v_mov_b32_e32 v77, v34
	v_mov_b32_e32 v78, v34
	v_mov_b32_e32 v79, v34
.LBB3_19:
	s_or_b64 exec, exec, s[4:5]
	s_waitcnt vmcnt(6)
	v_perm_b32 v112, v26, v26, s24
	v_perm_b32 v113, v26, v26, s25
	v_fma_mix_f32 v78, v112, v58, v78 op_sel_hi:[1,0,0]
	v_fma_mix_f32 v79, v113, v58, v79 op_sel_hi:[1,0,0]
	v_fma_mix_f32 v76, v112, v58, v76 op_sel:[1,0,0] op_sel_hi:[1,0,0]
	v_fma_mix_f32 v77, v113, v58, v77 op_sel:[1,0,0] op_sel_hi:[1,0,0]
	v_perm_b32 v114, v27, v27, s24
	v_perm_b32 v115, v27, v27, s25
	v_fma_mix_f32 v74, v114, v58, v74 op_sel_hi:[1,0,0]
	v_fma_mix_f32 v75, v115, v58, v75 op_sel_hi:[1,0,0]
	v_perm_b32 v116, v28, v28, s24
	v_perm_b32 v117, v28, v28, s25
	v_fma_mix_f32 v62, v116, v58, v70 op_sel_hi:[1,0,0]
	v_fma_mix_f32 v63, v117, v58, v71 op_sel_hi:[1,0,0]
	v_fma_mix_f32 v64, v116, v58, v68 op_sel:[1,0,0] op_sel_hi:[1,0,0]
	v_fma_mix_f32 v65, v117, v58, v69 op_sel:[1,0,0] op_sel_hi:[1,0,0]
	v_perm_b32 v118, v29, v29, s24
	v_perm_b32 v119, v29, v29, s25
	v_fma_mix_f32 v72, v114, v58, v72 op_sel:[1,0,0] op_sel_hi:[1,0,0]
	v_fma_mix_f32 v73, v115, v58, v73 op_sel:[1,0,0] op_sel_hi:[1,0,0]
	v_fma_mix_f32 v36, v118, v58, v66 op_sel_hi:[1,0,0]
	v_fma_mix_f32 v37, v119, v58, v67 op_sel_hi:[1,0,0]
	v_and_b32_e32 v28, 64, v52
	v_fma_mix_f32 v26, v118, v58, v34 op_sel:[1,0,0] op_sel_hi:[1,0,0]
	v_fma_mix_f32 v27, v119, v58, v35 op_sel:[1,0,0] op_sel_hi:[1,0,0]
	v_cmp_ne_u32_e64 s[0:1], 0, v28
	s_and_saveexec_b64 s[4:5], s[0:1]
	s_cbranch_execz .LBB3_21
	v_and_b32_e32 v28, 63, v98
	v_mul_u32_u24_e32 v28, 0x220, v28
	v_or_b32_e32 v42, v49, v28
	ds_read2_b32 v[28:29], v42 offset1:8
	ds_read2_b32 v[34:35], v42 offset0:16 offset1:24
	ds_read2_b32 v[58:59], v42 offset0:32 offset1:40
	s_waitcnt lgkmcnt(2)
	v_add_f32_e32 v28, v78, v28
	v_add_f32_e32 v29, v79, v29
	s_waitcnt lgkmcnt(1)
	v_add_f32_e32 v34, v76, v34
	ds_write2_b32 v42, v28, v29 offset1:8
	v_add_f32_e32 v28, v77, v35
	ds_write2_b32 v42, v34, v28 offset0:16 offset1:24
	ds_read2_b32 v[28:29], v42 offset0:48 offset1:56
	s_waitcnt lgkmcnt(3)
	v_add_f32_e32 v34, v74, v58
	v_add_f32_e32 v35, v75, v59
	ds_write2_b32 v42, v34, v35 offset0:32 offset1:40
	ds_read2_b32 v[34:35], v42 offset0:64 offset1:72
	s_waitcnt lgkmcnt(2)
	v_add_f32_e32 v28, v72, v28
	v_add_f32_e32 v29, v73, v29
	ds_write2_b32 v42, v28, v29 offset0:48 offset1:56
	ds_read2_b32 v[28:29], v42 offset0:80 offset1:88
	s_waitcnt lgkmcnt(2)
	v_add_f32_e32 v34, v62, v34
	v_add_f32_e32 v35, v63, v35
	ds_write2_b32 v42, v34, v35 offset0:64 offset1:72
	ds_read2_b32 v[34:35], v42 offset0:96 offset1:104
	s_waitcnt lgkmcnt(2)
	v_add_f32_e32 v28, v64, v28
	v_add_f32_e32 v29, v65, v29
	ds_write2_b32 v42, v28, v29 offset0:80 offset1:88
	ds_read2_b32 v[28:29], v42 offset0:112 offset1:120
	s_waitcnt lgkmcnt(2)
	v_add_f32_e32 v34, v36, v34
	ds_bpermute_b32 v36, v92, v95
	v_add_f32_e32 v35, v37, v35
	ds_write2_b32 v42, v34, v35 offset0:96 offset1:104
	s_waitcnt lgkmcnt(2)
	v_add_f32_e32 v26, v26, v28
	v_add_f32_e32 v27, v27, v29
	ds_write2_b32 v42, v26, v27 offset0:112 offset1:120
	v_mov_b32_e32 v26, 0
	s_waitcnt lgkmcnt(2)
	v_lshrrev_b32_e32 v98, 16, v36
	v_mov_b32_e32 v27, v26
	v_mov_b32_e32 v36, v26
	v_mov_b32_e32 v37, v26
	v_mov_b32_e32 v64, v26
	v_mov_b32_e32 v65, v26
	v_mov_b32_e32 v62, v26
	v_mov_b32_e32 v63, v26
	v_mov_b32_e32 v72, v26
	v_mov_b32_e32 v73, v26
	v_mov_b32_e32 v74, v26
	v_mov_b32_e32 v75, v26
	v_mov_b32_e32 v76, v26
	v_mov_b32_e32 v77, v26
	v_mov_b32_e32 v78, v26
	v_mov_b32_e32 v79, v26
.LBB3_21:
	s_or_b64 exec, exec, s[4:5]
	s_waitcnt vmcnt(5)
	v_perm_b32 v120, v23, v23, s24
	v_perm_b32 v121, v23, v23, s25
	v_perm_b32 v122, v22, v22, s24
	v_perm_b32 v123, v22, v22, s25
	v_fma_mix_f32 v22, v120, v54, v72 op_sel:[1,0,0] op_sel_hi:[1,0,0]
	v_fma_mix_f32 v23, v121, v54, v73 op_sel:[1,0,0] op_sel_hi:[1,0,0]
	v_perm_b32 v124, v24, v24, s24
	v_perm_b32 v125, v24, v24, s25
	v_fma_mix_f32 v62, v124, v54, v62 op_sel_hi:[1,0,0]
	v_fma_mix_f32 v63, v125, v54, v63 op_sel_hi:[1,0,0]
	v_fma_mix_f32 v68, v124, v54, v64 op_sel:[1,0,0] op_sel_hi:[1,0,0]
	v_fma_mix_f32 v69, v125, v54, v65 op_sel:[1,0,0] op_sel_hi:[1,0,0]
	v_perm_b32 v126, v25, v25, s24
	v_perm_b32 v127, v25, v25, s25
	v_fma_mix_f32 v36, v126, v54, v36 op_sel_hi:[1,0,0]
	v_fma_mix_f32 v37, v127, v54, v37 op_sel_hi:[1,0,0]
	v_fma_mix_f32 v24, v126, v54, v26 op_sel:[1,0,0] op_sel_hi:[1,0,0]
	v_fma_mix_f32 v25, v127, v54, v27 op_sel:[1,0,0] op_sel_hi:[1,0,0]
	v_and_b32_e32 v26, 0x80, v52
	v_fma_mix_f32 v28, v122, v54, v78 op_sel_hi:[1,0,0]
	v_fma_mix_f32 v29, v123, v54, v79 op_sel_hi:[1,0,0]
	v_fma_mix_f32 v34, v122, v54, v76 op_sel:[1,0,0] op_sel_hi:[1,0,0]
	v_fma_mix_f32 v35, v123, v54, v77 op_sel:[1,0,0] op_sel_hi:[1,0,0]
	v_fma_mix_f32 v58, v120, v54, v74 op_sel_hi:[1,0,0]
	v_fma_mix_f32 v59, v121, v54, v75 op_sel_hi:[1,0,0]
	v_cmp_ne_u32_e64 s[0:1], 0, v26
	s_and_saveexec_b64 s[4:5], s[0:1]
	s_cbranch_execz .LBB3_6
	v_and_b32_e32 v26, 63, v98
	v_mul_u32_u24_e32 v26, 0x220, v26
	v_or_b32_e32 v42, v49, v26
	ds_read2_b32 v[26:27], v42 offset1:8
	ds_read2_b32 v[52:53], v42 offset0:16 offset1:24
	ds_read2_b32 v[64:65], v42 offset0:32 offset1:40
	s_waitcnt lgkmcnt(2)
	v_add_f32_e32 v26, v28, v26
	v_add_f32_e32 v27, v29, v27
	s_waitcnt lgkmcnt(1)
	v_add_f32_e32 v28, v34, v52
	ds_write2_b32 v42, v26, v27 offset1:8
	v_add_f32_e32 v26, v35, v53
	ds_write2_b32 v42, v28, v26 offset0:16 offset1:24
	ds_read2_b32 v[26:27], v42 offset0:48 offset1:56
	s_waitcnt lgkmcnt(3)
	v_add_f32_e32 v28, v58, v64
	v_add_f32_e32 v29, v59, v65
	ds_write2_b32 v42, v28, v29 offset0:32 offset1:40
	ds_read2_b32 v[28:29], v42 offset0:64 offset1:72
	s_waitcnt lgkmcnt(2)
	v_add_f32_e32 v22, v22, v26
	v_add_f32_e32 v23, v23, v27
	ds_write2_b32 v42, v22, v23 offset0:48 offset1:56
	ds_read2_b32 v[22:23], v42 offset0:80 offset1:88
	s_waitcnt lgkmcnt(2)
	v_add_f32_e32 v26, v62, v28
	v_add_f32_e32 v27, v63, v29
	ds_write2_b32 v42, v26, v27 offset0:64 offset1:72
	ds_read2_b32 v[26:27], v42 offset0:96 offset1:104
	s_waitcnt lgkmcnt(2)
	v_add_f32_e32 v22, v68, v22
	v_add_f32_e32 v23, v69, v23
	ds_write2_b32 v42, v22, v23 offset0:80 offset1:88
	ds_read2_b32 v[22:23], v42 offset0:112 offset1:120
	ds_bpermute_b32 v28, v93, v95
	s_waitcnt lgkmcnt(3)
	v_add_f32_e32 v26, v36, v26
	v_add_f32_e32 v27, v37, v27
	ds_write2_b32 v42, v26, v27 offset0:96 offset1:104
	s_waitcnt lgkmcnt(2)
	v_add_f32_e32 v22, v24, v22
	v_add_f32_e32 v23, v25, v23
	v_mov_b32_e32 v24, 0
	ds_write2_b32 v42, v22, v23 offset0:112 offset1:120
	s_waitcnt lgkmcnt(2)
	v_lshrrev_b32_e32 v98, 16, v28
	v_mov_b32_e32 v25, v24
	v_mov_b32_e32 v36, v24
	v_mov_b32_e32 v37, v24
	v_mov_b32_e32 v68, v24
	v_mov_b32_e32 v69, v24
	v_mov_b32_e32 v62, v24
	v_mov_b32_e32 v63, v24
	v_mov_b32_e32 v22, v24
	v_mov_b32_e32 v23, v24
	v_mov_b32_e32 v58, v24
	v_mov_b32_e32 v59, v24
	v_mov_b32_e32 v34, v24
	v_mov_b32_e32 v35, v24
	v_mov_b32_e32 v28, v24
	v_mov_b32_e32 v29, v24
	s_branch .LBB3_6

	.amdhsa_kernel _Z8k_layer2PKhPKfPK15HIP_vector_typeIjLj4EEPKjS2_PKDF16_S2_Pf
		.amdhsa_group_segment_fixed_size 39168
		.amdhsa_private_segment_fixed_size 0
		.amdhsa_kernarg_size 64
		.amdhsa_user_sgpr_count 2
		.amdhsa_user_sgpr_dispatch_ptr 0
		.amdhsa_user_sgpr_queue_ptr 0
		.amdhsa_user_sgpr_kernarg_segment_ptr 1
		.amdhsa_user_sgpr_dispatch_id 0
		.amdhsa_user_sgpr_kernarg_preload_length 0
		.amdhsa_user_sgpr_kernarg_preload_offset 0
		.amdhsa_user_sgpr_private_segment_size 0
		.amdhsa_uses_dynamic_stack 0
		.amdhsa_enable_private_segment 0
		.amdhsa_system_sgpr_workgroup_id_x 1
		.amdhsa_system_sgpr_workgroup_id_y 0
		.amdhsa_system_sgpr_workgroup_id_z 0
		.amdhsa_system_sgpr_workgroup_info 0
		.amdhsa_system_vgpr_workitem_id 0
		.amdhsa_next_free_vgpr 128
		.amdhsa_next_free_sgpr 96
		.amdhsa_accum_offset 128
		.amdhsa_reserve_vcc 1
		.amdhsa_float_round_mode_32 0
		.amdhsa_float_round_mode_16_64 0
		.amdhsa_float_denorm_mode_32 3
		.amdhsa_float_denorm_mode_16_64 3
		.amdhsa_dx10_clamp 1
		.amdhsa_ieee_mode 1
		.amdhsa_fp16_overflow 0
		.amdhsa_tg_split 0
		.amdhsa_exception_fp_ieee_invalid_op 0
		.amdhsa_exception_fp_denorm_src 0
		.amdhsa_exception_fp_ieee_div_zero 0
		.amdhsa_exception_fp_ieee_overflow 0
		.amdhsa_exception_fp_ieee_underflow 0
		.amdhsa_exception_fp_ieee_inexact 0
		.amdhsa_exception_int_div_zero 0
	.end_amdhsa_kernel

amdhsa.kernels:
  - .agpr_count:     0
    .args:
      - .actual_access:  read_only
        .address_space:  global
        .offset:         0
        .size:           8
        .value_kind:     global_buffer
      - .actual_access:  read_only
        .address_space:  global
        .offset:         8
        .size:           8
        .value_kind:     global_buffer
      - .actual_access:  write_only
        .address_space:  global
        .offset:         16
        .size:           8
        .value_kind:     global_buffer
      - .actual_access:  write_only
        .address_space:  global
        .offset:         24
        .size:           8
        .value_kind:     global_buffer
      - .actual_access:  read_only
        .address_space:  global
        .offset:         32
        .size:           8
        .value_kind:     global_buffer
      - .actual_access:  read_only
        .address_space:  global
        .offset:         40
        .size:           8
        .value_kind:     global_buffer
      - .actual_access:  read_only
        .address_space:  global
        .offset:         48
        .size:           8
        .value_kind:     global_buffer
      - .actual_access:  read_only
        .address_space:  global
        .offset:         56
        .size:           8
        .value_kind:     global_buffer
      - .actual_access:  read_only
        .address_space:  global
        .offset:         64
        .size:           8
        .value_kind:     global_buffer
      - .actual_access:  write_only
        .address_space:  global
        .offset:         72
        .size:           8
        .value_kind:     global_buffer
      - .actual_access:  write_only
        .address_space:  global
        .offset:         80
        .size:           8
        .value_kind:     global_buffer
      - .actual_access:  write_only
        .address_space:  global
        .offset:         88
        .size:           8
        .value_kind:     global_buffer
      - .actual_access:  write_only
        .address_space:  global
        .offset:         96
        .size:           8
        .value_kind:     global_buffer
      - .actual_access:  write_only
        .address_space:  global
        .offset:         104
        .size:           8
        .value_kind:     global_buffer
      - .actual_access:  write_only
        .address_space:  global
        .offset:         112
        .size:           8
        .value_kind:     global_buffer
      - .offset:         120
        .size:           4
        .value_kind:     hidden_block_count_x
      - .offset:         124
        .size:           4
        .value_kind:     hidden_block_count_y
      - .offset:         128
        .size:           4
        .value_kind:     hidden_block_count_z
      - .offset:         132
        .size:           2
        .value_kind:     hidden_group_size_x
      - .offset:         134
        .size:           2
        .value_kind:     hidden_group_size_y
      - .offset:         136
        .size:           2
        .value_kind:     hidden_group_size_z
      - .offset:         138
        .size:           2
        .value_kind:     hidden_remainder_x
      - .offset:         140
        .size:           2
        .value_kind:     hidden_remainder_y
      - .offset:         142
        .size:           2
        .value_kind:     hidden_remainder_z
      - .offset:         160
        .size:           8
        .value_kind:     hidden_global_offset_x
      - .offset:         168
        .size:           8
        .value_kind:     hidden_global_offset_y
      - .offset:         176
        .size:           8
        .value_kind:     hidden_global_offset_z
      - .offset:         184
        .size:           2
        .value_kind:     hidden_grid_dims
    .group_segment_fixed_size: 21520
    .kernarg_segment_align: 8
    .kernarg_segment_size: 376
    .language:       OpenCL C
    .language_version:
      - 2
      - 0
    .max_flat_workgroup_size: 1024
    .name:           _Z11k_chunksortPKiS0_PjS1_PKfS3_S3_S3_S3_PDF16_S4_PfS5_S4_Ph
    .private_segment_fixed_size: 0
    .sgpr_count:     32
    .sgpr_spill_count: 0
    .symbol:         _Z11k_chunksortPKiS0_PjS1_PKfS3_S3_S3_S3_PDF16_S4_PfS5_S4_Ph.kd
    .uniform_work_group_size: 1
    .uses_dynamic_stack: false
    .vgpr_count:     38
    .vgpr_spill_count: 0
    .wavefront_size: 64
  - .agpr_count:     0
    .args:
      - .actual_access:  read_only
        .address_space:  global
        .offset:         0
        .size:           8
        .value_kind:     global_buffer
      - .actual_access:  read_only
        .address_space:  global
        .offset:         8
        .size:           8
        .value_kind:     global_buffer
      - .actual_access:  read_only
        .address_space:  global
        .offset:         16
        .size:           8
        .value_kind:     global_buffer
      - .actual_access:  write_only
        .address_space:  global
        .offset:         24
        .size:           8
        .value_kind:     global_buffer
      - .actual_access:  write_only
        .address_space:  global
        .offset:         32
        .size:           8
        .value_kind:     global_buffer
      - .actual_access:  write_only
        .address_space:  global
        .offset:         40
        .size:           8
        .value_kind:     global_buffer
      - .actual_access:  write_only
        .address_space:  global
        .offset:         48
        .size:           8
        .value_kind:     global_buffer
    .group_segment_fixed_size: 22536
    .kernarg_segment_align: 8
    .kernarg_segment_size: 56
    .language:       OpenCL C
    .language_version:
      - 2
      - 0
    .max_flat_workgroup_size: 1024
    .name:           _Z5k_csrPKjS0_PKfPjPfPDF16_P15HIP_vector_typeIjLj4EE
    .private_segment_fixed_size: 0
    .sgpr_count:     44
    .sgpr_spill_count: 0
    .symbol:         _Z5k_csrPKjS0_PKfPjPfPDF16_P15HIP_vector_typeIjLj4EE.kd
    .uniform_work_group_size: 1
    .uses_dynamic_stack: false
    .vgpr_count:     48
    .vgpr_spill_count: 0
    .wavefront_size: 64
  - .agpr_count:     0
    .args:
      - .actual_access:  read_only
        .address_space:  global
        .offset:         0
        .size:           8
        .value_kind:     global_buffer
      - .actual_access:  read_only
        .address_space:  global
        .offset:         8
        .size:           8
        .value_kind:     global_buffer
      - .actual_access:  read_only
        .address_space:  global
        .offset:         16
        .size:           8
        .value_kind:     global_buffer
      - .actual_access:  read_only
        .address_space:  global
        .offset:         24
        .size:           8
        .value_kind:     global_buffer
      - .actual_access:  read_only
        .address_space:  global
        .offset:         32
        .size:           8
        .value_kind:     global_buffer
      - .actual_access:  read_only
        .address_space:  global
        .offset:         40
        .size:           8
        .value_kind:     global_buffer
      - .actual_access:  read_only
        .address_space:  global
        .offset:         48
        .size:           8
        .value_kind:     global_buffer
      - .actual_access:  write_only
        .address_space:  global
        .offset:         56
        .size:           8
        .value_kind:     global_buffer
      - .actual_access:  write_only
        .address_space:  global
        .offset:         64
        .size:           8
        .value_kind:     global_buffer
    .group_segment_fixed_size: 36112
    .kernarg_segment_align: 8
    .kernarg_segment_size: 72
    .language:       OpenCL C
    .language_version:
      - 2
      - 0
    .max_flat_workgroup_size: 256
    .name:           _Z8k_layer1PKfPKDF16_PK15HIP_vector_typeIjLj4EEPKjS0_S2_S0_PhPf
    .private_segment_fixed_size: 0
    .sgpr_count:     30
    .sgpr_spill_count: 0
    .symbol:         _Z8k_layer1PKfPKDF16_PK15HIP_vector_typeIjLj4EEPKjS0_S2_S0_PhPf.kd
    .uniform_work_group_size: 1
    .uses_dynamic_stack: false
    .vgpr_count:     128
    .vgpr_spill_count: 0
    .wavefront_size: 64
  - .agpr_count:     0
    .args:
      - .actual_access:  read_only
        .address_space:  global
        .offset:         0
        .size:           8
        .value_kind:     global_buffer
      - .actual_access:  read_only
        .address_space:  global
        .offset:         8
        .size:           8
        .value_kind:     global_buffer
      - .actual_access:  read_only
        .address_space:  global
        .offset:         16
        .size:           8
        .value_kind:     global_buffer
      - .actual_access:  read_only
        .address_space:  global
        .offset:         24
        .size:           8
        .value_kind:     global_buffer
      - .actual_access:  read_only
        .address_space:  global
        .offset:         32
        .size:           8
        .value_kind:     global_buffer
      - .actual_access:  read_only
        .address_space:  global
        .offset:         40
        .size:           8
        .value_kind:     global_buffer
      - .actual_access:  read_only
        .address_space:  global
        .offset:         48
        .size:           8
        .value_kind:     global_buffer
      - .address_space:  global
        .offset:         56
        .size:           8
        .value_kind:     global_buffer
    .group_segment_fixed_size: 39168
    .kernarg_segment_align: 8
    .kernarg_segment_size: 64
    .language:       OpenCL C
    .language_version:
      - 2
      - 0
    .max_flat_workgroup_size: 256
    .name:           _Z8k_layer2PKhPKfPK15HIP_vector_typeIjLj4EEPKjS2_PKDF16_S2_Pf
    .private_segment_fixed_size: 0
    .sgpr_count:     27
    .sgpr_spill_count: 0
    .symbol:         _Z8k_layer2PKhPKfPK15HIP_vector_typeIjLj4EEPKjS2_PKDF16_S2_Pf.kd
    .uniform_work_group_size: 1
    .uses_dynamic_stack: false
    .vgpr_count:     128
    .vgpr_spill_count: 0
    .wavefront_size: 64
  - .agpr_count:     0
    .args:
      - .actual_access:  read_only
        .address_space:  global
        .offset:         0
        .size:           8
        .value_kind:     global_buffer
      - .actual_access:  read_only
        .address_space:  global
        .offset:         8
        .size:           8
        .value_kind:     global_buffer
      - .actual_access:  read_only
        .address_space:  global
        .offset:         16
        .size:           8
        .value_kind:     global_buffer
      - .actual_access:  read_only
        .address_space:  global
        .offset:         24
        .size:           8
        .value_kind:     global_buffer
      - .actual_access:  read_only
        .address_space:  global
        .offset:         32
        .size:           8
        .value_kind:     global_buffer
      - .actual_access:  write_only
        .address_space:  global
        .offset:         40
        .size:           8
        .value_kind:     global_buffer
    .group_segment_fixed_size: 512
    .kernarg_segment_align: 8
    .kernarg_segment_size: 48
    .language:       OpenCL C
    .language_version:
      - 2
      - 0
    .max_flat_workgroup_size: 320
    .name:           _Z7k_headsPKfS0_S0_S0_S0_Pf
    .private_segment_fixed_size: 0
    .sgpr_count:     18
    .sgpr_spill_count: 0
    .symbol:         _Z7k_headsPKfS0_S0_S0_S0_Pf.kd
    .uniform_work_group_size: 1
    .uses_dynamic_stack: false
    .vgpr_count:     56
    .vgpr_spill_count: 0
    .wavefront_size: 64
